# v8 + 4-bit XOR swizzle of the K tile in LDS (bank-conflict-free ds_read_b128 fragment reads; LDS-DMA lane mapping and tile-0 staging store adjusted to match); next_free_vgpr 256 for four persistent fr
# speedup vs baseline: 1.0257x; 1.0092x over previous
.LBB0_1086:
	v_mbcnt_lo_u32_b32 v146, -1, 0
	v_mbcnt_hi_u32_b32 v146, -1, v146
	s_and_b64 s[2:3], s[4:5], exec
	v_ashrrev_i32_e32 v4, 5, v146
	v_ashrrev_i32_e32 v11, 4, v146
	v_and_b32_e32 v13, 15, v146
	v_lshrrev_b32_e32 v0, 1, v146
	v_mov_b32_e32 v7, s56
	v_lshlrev_b32_e32 v7, 1, v7
	v_and_b32_e32 v7, 8, v7
	v_or_b32_e32 v7, v7, v11
	v_xor_b32_e32 v7, v7, v13
	v_add_u32_e32 v8, s56, v4
	v_bfe_u32 v2, v146, 2, 2
	v_and_b32_e32 v5, 8, v0
	v_lshlrev_b32_e32 v10, 4, v7
	v_lshlrev_b32_e32 v7, 1, v8
	v_or_b32_e32 v14, v5, v2
	v_and_b32_e32 v7, -16, v7
	v_and_b32_e32 v8, 4, v8
	v_lshlrev_b32_e32 v12, 4, v146
	v_or3_b32 v15, v8, v7, v14
	v_lshlrev_b32_e32 v9, 6, v4
	v_and_b32_e32 v3, 48, v12
	v_and_b32_e32 v9, 0xc0, v9
	v_lshlrev_b32_e32 v15, 12, v15
	v_or3_b32 v19, v15, v9, v3
	v_add_u32_e32 v15, s57, v11
	v_lshlrev_b32_e32 v6, 12, v11
	v_bitop3_b32 v11, v15, v13, 15 bitop3:0x6c
	v_lshlrev_b32_e32 v11, 4, v11
	s_cselect_b32 s6, s76, s77
	v_lshl_or_b32 v13, v15, 12, v11
	v_add_u32_e32 v15, s58, v4
	s_or_b32 s44, s6, 0x80
	v_lshlrev_b32_e32 v16, 1, v15
	s_add_u32 s2, s71, s44
	v_and_b32_e32 v16, 0xffff0, v16
	v_and_b32_e32 v17, 4, v15
	s_addc_u32 s3, s70, 0
	v_or3_b32 v14, v17, v16, v14
	v_lshlrev_b32_e32 v15, 6, v15
	s_lshl_b64 s[36:37], s[2:3], 12
	v_and_b32_e32 v145, 31, v146
	v_and_b32_e32 v15, 0xc0, v15
	v_lshlrev_b32_e32 v14, 12, v14
	s_add_u32 s2, s79, s36
	v_or3_b32 v20, v14, v15, v3
	v_or_b32_e32 v14, s8, v145
	s_addc_u32 s3, s81, s37
	v_ashrrev_i32_e32 v15, 31, v14
	s_add_i32 s7, s6, 0x17f
	v_lshlrev_b64 v[14:15], 12, v[14:15]
	v_lshlrev_b32_e32 v16, 3, v4
	s_and_b32 s38, s7, 0x1f40
	v_lshl_add_u64 v[14:15], s[2:3], 0, v[14:15]
	v_ashrrev_i32_e32 v17, 31, v16
	s_lshl_b32 s33, s38, 12
	v_lshl_add_u64 v[14:15], v[16:17], 1, v[14:15]
	s_add_u32 s2, s82, s33
	global_load_dwordx4 v[112:115], v[14:15], off
	global_load_dwordx4 v[116:119], v[14:15], off offset:32
	global_load_dwordx4 v[120:123], v[14:15], off offset:64
	global_load_dwordx4 v[124:127], v[14:15], off offset:96
	global_load_dwordx4 v[128:131], v[14:15], off offset:128
	global_load_dwordx4 v[132:135], v[14:15], off offset:160
	global_load_dwordx4 v[136:139], v[14:15], off offset:192
	global_load_dwordx4 v[140:143], v[14:15], off offset:224
	s_addc_u32 s3, s83, 0
	s_add_u32 s34, s84, s33
	v_add_u32_e32 v0, s55, v6
	s_addc_u32 s35, s85, 0
	s_add_i32 s33, s68, 0x8000
	v_or_b32_e32 v18, v10, v0
	s_mov_b32 m0, s33
	v_add_u32_e32 v14, s38, v146
	global_load_lds_dwordx4 v18, s[2:3]
	s_mov_b32 m0, s68
	s_add_i32 s42, s68, 0x8400
	v_ashrrev_i32_e32 v15, 31, v14
	global_load_lds_dwordx4 v19, s[34:35]
	s_mov_b32 m0, s42
	s_add_i32 s43, s68, 0x400
	v_lshl_add_u64 v[14:15], v[14:15], 2, s[30:31]
	global_load_lds_dwordx4 v13, s[2:3]
	s_mov_b32 m0, s43
	global_load_dword v172, v[14:15], off
	v_cmp_ne_u32_e64 s[2:3], 1, v158
	global_load_lds_dwordx4 v20, s[34:35]
	s_andn2_b64 vcc, exec, s[10:11]
	s_cbranch_vccnz .LBB0_1088
	v_lshl_add_u32 v13, v146, 2, 0
	v_add_u32_e32 v13, 0x10800, v13
	s_waitcnt vmcnt(0)
	ds_write_b32 v13, v172
.LBB0_1088:
	v_lshlrev_b32_e32 v13, 3, v146
	v_and_b32_e32 v12, 0xc0, v12
	v_lshlrev_b32_e32 v14, 1, v146
	s_xor_b64 s[34:35], s[4:5], -1
	v_and_or_b32 v12, v13, 24, v12
	v_and_b32_e32 v14, 32, v14
	v_and_b32_e32 v13, 0x100, v13
	s_add_i32 s44, s44, s8
	v_or3_b32 v12, v12, v14, v13
	v_or_b32_e32 v13, s44, v145
	s_cmp_lg_u32 0, -1
	s_cselect_b32 s4, 0, 0
	s_lshr_b32 s46, s7, 6
	v_add_u32_e32 v163, 0xffffff91, v13
	v_lshlrev_b32_e32 v164, 4, v4
	v_lshlrev_b32_e32 v13, 4, v145
	s_add_i32 s38, 0, 0x10800
	s_add_i32 s47, s46, -2
	s_or_b32 s64, s44, 31
	v_and_b32_e32 v13, 0x70, v13
	v_add_u32_e32 v14, 32, v164
	v_lshl_add_u32 v171, v146, 2, s38
	s_lshl_b32 s38, s46, 8
	v_xad_u32 v168, v14, v13, 0
	v_add_u32_e32 v14, 64, v164
	s_add_u32 s38, s89, s38
	v_xad_u32 v169, v14, v13, 0
	v_add_u32_e32 v14, 0x60, v164
	s_addc_u32 s39, s88, 0
	s_and_b32 s7, s7, 0x1fc0
	s_add_i32 s6, s60, s6
	v_lshlrev_b32_e32 v144, 2, v4
	v_xad_u32 v166, v13, v164, 0
	v_xad_u32 v170, v14, v13, 0
	s_sub_i32 s65, s7, 64
	v_add_u32_e32 v13, s6, v145
	s_lshl_b32 s6, s46, 18
	v_ashrrev_i32_e32 v147, 31, v146
	v_sub_u32_e32 v13, v13, v144
	s_add_u32 s6, s90, s6
	v_lshl_add_u64 v[148:149], v[146:147], 2, s[38:39]
	v_subrev_u32_e32 v147, s7, v13
	s_addc_u32 s7, s91, 0
	v_add_u32_e32 v0, v0, v10
	v_lshl_add_u64 v[150:151], s[6:7], 0, v[0:1]
	v_add3_u32 v0, s61, v6, v11
	v_lshl_add_u64 v[152:153], s[6:7], 0, v[0:1]
	v_add_u32_e32 v0, v7, v5
	v_add3_u32 v0, v0, v8, v2
	v_lshl_or_b32 v0, v0, 12, v9
	v_add_u32_e32 v0, v0, v3
	v_lshl_add_u64 v[154:155], s[6:7], 0, v[0:1]
	v_add_u32_e32 v0, s62, v4
	v_lshlrev_b32_e32 v4, 1, v0
	s_mov_b32 s38, 0xffff0
	v_and_or_b32 v4, v4, s38, v5
	v_and_b32_e32 v0, 4, v0
	v_add_u32_e32 v162, s4, v12
	v_lshrrev_b32_e32 v12, 5, v146
	v_add_u32_e32 v0, v4, v0
	v_add_lshl_u32 v0, v0, v2, 12
	v_add_u16_e32 v2, 2, v12
	v_and_b32_e32 v2, 3, v2
	v_lshlrev_b32_e32 v2, 6, v2
	s_waitcnt vmcnt(0)
	v_or3_b32 v0, v0, v2, v3
	v_mov_b32_e32 v14, v1
	v_mov_b32_e32 v15, v1
	v_lshl_add_u64 v[156:157], s[6:7], 0, v[0:1]
	v_mov_b32_e32 v0, v1
	v_mov_b32_e32 v2, v1
	v_mov_b32_e32 v3, v1
	v_mov_b32_e32 v4, v1
	v_mov_b32_e32 v5, v1
	v_mov_b32_e32 v6, v1
	v_mov_b32_e32 v7, v1
	v_mov_b32_e32 v8, v1
	v_mov_b32_e32 v9, v1
	v_mov_b32_e32 v10, v1
	v_mov_b32_e32 v11, v1
	v_mov_b32_e32 v12, v1
	v_mov_b32_e32 v13, v1
	s_waitcnt lgkmcnt(0)
	v_mov_b64_e32 v[30:31], v[14:15]
	v_mov_b64_e32 v[46:47], v[14:15]
	v_mov_b64_e32 v[62:63], v[14:15]
	v_mov_b64_e32 v[78:79], v[14:15]
	s_mov_b32 s45, 0
	v_lshlrev_b32_e32 v165, 8, v145
	v_cmp_gt_u32_e64 s[4:5], 32, v146
	v_lshl_add_u32 v167, v145, 2, s54
	v_add_u32_e32 v161, s54, v164
	v_mov_b32_e32 v174, 0
	v_mov_b32_e32 v173, 0xf149f2ca
	s_mov_b32 s66, s46
	v_mov_b64_e32 v[28:29], v[12:13]
	v_mov_b64_e32 v[26:27], v[10:11]
	v_mov_b64_e32 v[24:25], v[8:9]
	v_mov_b64_e32 v[22:23], v[6:7]
	v_mov_b64_e32 v[20:21], v[4:5]
	v_mov_b64_e32 v[18:19], v[2:3]
	v_mov_b64_e32 v[16:17], v[0:1]
	v_mov_b64_e32 v[44:45], v[12:13]
	v_mov_b64_e32 v[42:43], v[10:11]
	v_mov_b64_e32 v[40:41], v[8:9]
	v_mov_b64_e32 v[38:39], v[6:7]
	v_mov_b64_e32 v[36:37], v[4:5]
	v_mov_b64_e32 v[34:35], v[2:3]
	v_mov_b64_e32 v[32:33], v[0:1]
	v_mov_b64_e32 v[60:61], v[12:13]
	v_mov_b64_e32 v[58:59], v[10:11]
	v_mov_b64_e32 v[56:57], v[8:9]
	v_mov_b64_e32 v[54:55], v[6:7]
	v_mov_b64_e32 v[52:53], v[4:5]
	v_mov_b64_e32 v[50:51], v[2:3]
	v_mov_b64_e32 v[48:49], v[0:1]
	v_mov_b64_e32 v[76:77], v[12:13]
	v_mov_b64_e32 v[74:75], v[10:11]
	v_mov_b64_e32 v[72:73], v[8:9]
	v_mov_b64_e32 v[70:71], v[6:7]
	v_mov_b64_e32 v[68:69], v[4:5]
	v_mov_b64_e32 v[66:67], v[2:3]
	v_mov_b64_e32 v[64:65], v[0:1]
	s_waitcnt vmcnt(0)
	s_barrier
	s_mov_b32 s45, 0
	s_lshl_b32 s65, s46, 6
	s_mov_b32 s66, 0
	s_mov_b32 s33, 0x8000
	s_mov_b32 s42, 0x11000
	s_mov_b32 s43, 0x15000
	s_mov_b32 s47, 0x19000
	s_mov_b32 s99, 0
	v_subrev_u32_e32 v147, 64, v147
	v_lshlrev_b32_e32 v232, 2, v146
	s_lshr_b32 s6, s68, 11
	s_and_b32 s7, s6, 3
	s_lshl_b32 s98, s7, 12
	s_lshl_b32 s7, s7, 16
	s_add_i32 s40, s46, -1
	s_lshl_b32 s41, s40, 8
	s_lshl_b32 s39, s40, 18
	s_add_u32 s40, s30, s41
	s_addc_u32 s41, s31, 0
	s_add_u32 s39, s39, s7
	v_and_b32_e32 v0, 15, v145
	v_lshlrev_b32_e32 v0, 4, v0
	v_xor_b32_e32 v0, v0, v164
	v_xad_u32 v166, v0, 0, v165
	v_xad_u32 v168, v0, 32, v165
	v_xad_u32 v169, v0, 64, v165
	s_movk_i32 s7, 0x60
	v_xad_u32 v170, v0, s7, v165
	s_movk_i32 s7, 0x80
	v_xad_u32 v251, v0, s7, v165
	s_movk_i32 s7, 0xa0
	v_xad_u32 v252, v0, s7, v165
	s_movk_i32 s7, 0xc0
	v_xad_u32 v253, v0, s7, v165
	s_movk_i32 s7, 0xe0
	v_xad_u32 v254, v0, s7, v165
	s_cmp_ge_u32 s6, 4
	s_cbranch_scc0 .Lat_setup_done
	s_add_u32 s100, s82, s39
	s_addc_u32 s101, s83, 0
	s_add_u32 s38, s84, s39
	s_addc_u32 s39, s85, 0
	v_lshrrev_b32_e32 v0, 4, v146
	v_and_b32_e32 v2, 15, v146
	v_xor_b32_e32 v2, v2, v0
	v_lshlrev_b32_e32 v2, 4, v2
	v_lshl_add_u32 v14, v0, 12, v2
	v_xor_b32_e32 v15, 64, v14
	v_add_u32_e32 v15, 0x4000, v15
	v_xor_b32_e32 v175, 0x80, v14
	v_add_u32_e32 v175, 0x8000, v175
	v_xor_b32_e32 v155, 0xc0, v14
	v_add_u32_e32 v155, 0xc000, v155
	v_bfe_u32 v0, v146, 4, 1
	v_bfe_u32 v2, v146, 2, 2
	v_lshl_add_u32 v0, v0, 3, v2
	v_lshlrev_b32_e32 v0, 12, v0
	v_lshrrev_b32_e32 v2, 5, v146
	v_lshl_add_u32 v0, v2, 6, v0
	v_and_b32_e32 v2, 3, v146
	v_lshl_add_u32 v228, v2, 4, v0
	v_add_u32_e32 v229, 0x80, v228
	v_add_u32_e32 v230, 0x4000, v228
	v_add_u32_e32 v231, 0x4080, v228
	s_add_i32 s6, s98, 0x4000
	s_mov_b32 s7, s6
	s_mov_b32 m0, s7
	s_add_i32 s7, s7, 0x400
	global_load_lds_dwordx4 v228, s[38:39]
	s_mov_b32 m0, s7
	s_add_i32 s7, s7, 0x400
	global_load_lds_dwordx4 v229, s[38:39]
	s_mov_b32 m0, s7
	s_add_i32 s7, s7, 0x400
	global_load_lds_dwordx4 v230, s[38:39]
	s_mov_b32 m0, s7
	s_nop 0
	global_load_lds_dwordx4 v231, s[38:39]
	s_sub_u32 s38, s38, 0x40000
	s_subb_u32 s39, s39, 0
	s_add_i32 s6, s42, s98
	s_mov_b32 s7, s6
	s_mov_b32 m0, s7
	s_add_i32 s7, s7, 0x400
	global_load_lds_dwordx4 v14, s[100:101]
	s_mov_b32 m0, s7
	s_add_i32 s7, s7, 0x400
	global_load_lds_dwordx4 v15, s[100:101]
	s_mov_b32 m0, s7
	s_add_i32 s7, s7, 0x400
	global_load_lds_dwordx4 v175, s[100:101]
	s_mov_b32 m0, s7
	s_nop 0
	global_load_lds_dwordx4 v155, s[100:101]
	global_load_dword v154, v232, s[40:41]
	s_sub_u32 s100, s100, 0x40000
	s_subb_u32 s101, s101, 0
	s_sub_u32 s40, s40, 0x100
	s_subb_u32 s41, s41, 0
	s_add_i32 s6, s43, s98
	s_mov_b32 s7, s6
	s_mov_b32 m0, s7
	s_add_i32 s7, s7, 0x400
	global_load_lds_dwordx4 v14, s[100:101]
	s_mov_b32 m0, s7
	s_add_i32 s7, s7, 0x400
	global_load_lds_dwordx4 v15, s[100:101]
	s_mov_b32 m0, s7
	s_add_i32 s7, s7, 0x400
	global_load_lds_dwordx4 v175, s[100:101]
	s_mov_b32 m0, s7
	s_nop 0
	global_load_lds_dwordx4 v155, s[100:101]
	global_load_dword v172, v232, s[40:41]
	s_sub_u32 s100, s100, 0x40000
	s_subb_u32 s101, s101, 0
	s_sub_u32 s40, s40, 0x100
	s_subb_u32 s41, s41, 0
	s_add_i32 s6, s47, s98
	s_mov_b32 s7, s6
	s_mov_b32 m0, s7
	s_add_i32 s7, s7, 0x400
	global_load_lds_dwordx4 v14, s[100:101]
	s_mov_b32 m0, s7
	s_add_i32 s7, s7, 0x400
	global_load_lds_dwordx4 v15, s[100:101]
	s_mov_b32 m0, s7
	s_add_i32 s7, s7, 0x400
	global_load_lds_dwordx4 v175, s[100:101]
	s_mov_b32 m0, s7
	s_nop 0
	global_load_lds_dwordx4 v155, s[100:101]
	global_load_dword v156, v232, s[40:41]
	s_sub_u32 s100, s100, 0x40000
	s_subb_u32 s101, s101, 0
	s_sub_u32 s40, s40, 0x100
	s_subb_u32 s41, s41, 0
	s_waitcnt vmcnt(0)
	s_cmp_lg_u32 s68, 0x2000
	s_cbranch_scc1 .Lat_setup_done
	v_add_u32_e32 v0, 256, v171
	ds_write_b32 v0, v154
	v_add_u32_e32 v0, 512, v171
	ds_write_b32 v0, v172
	v_add_u32_e32 v0, 768, v171
	ds_write_b32 v0, v156
	s_waitcnt lgkmcnt(0)
.Lat_setup_done:
	s_barrier
	s_cmp_gt_i32 s65, s64
	s_cbranch_scc1 .Lat_tile0
	v_add_u32_e32 v246, s33, v166
	v_add_u32_e32 v247, s33, v168
	v_add_u32_e32 v248, s33, v169
	v_add_u32_e32 v249, s33, v170
	ds_read_b128 v[208:211], v246
	ds_read_b128 v[212:215], v246 offset:8192
	ds_read_b128 v[216:219], v247
	ds_read_b128 v[220:223], v247 offset:8192
	ds_read_b128 v[224:227], v248
	ds_read_b128 v[234:237], v248 offset:8192
	ds_read_b128 v[238:241], v249
	ds_read_b128 v[242:245], v249 offset:8192
	v_add_u32_e32 v246, s33, v251
	v_add_u32_e32 v247, s33, v252
	v_add_u32_e32 v248, s33, v253
	v_add_u32_e32 v249, s33, v254
	s_add_i32 s6, s45, 0
	s_and_b32 s6, s6, 3
	s_lshl_b32 s6, s6, 8
	s_add_i32 s6, s6, 0x10800
	v_add_u32_e32 v152, s6, v164
	ds_read_b128 v[96:99], v152
	ds_read_b128 v[100:103], v152 offset:32
	ds_read_b128 v[80:83], v152 offset:128
	ds_read_b128 v[84:87], v152 offset:160
	ds_read_b128 v[104:107], v152 offset:64
	ds_read_b128 v[108:111], v152 offset:96
	ds_read_b128 v[88:91], v152 offset:192
	ds_read_b128 v[92:95], v152 offset:224
	s_waitcnt lgkmcnt(0)
	v_mfma_f32_32x32x16_bf16 v[96:111], v[208:211], v[112:115], v[96:111]
	ds_read_b128 v[208:211], v246
	v_mfma_f32_32x32x16_bf16 v[80:95], v[212:215], v[112:115], v[80:95]
	ds_read_b128 v[212:215], v246 offset:8192
	v_mfma_f32_32x32x16_bf16 v[96:111], v[216:219], v[116:119], v[96:111]
	ds_read_b128 v[216:219], v247
	v_mfma_f32_32x32x16_bf16 v[80:95], v[220:223], v[116:119], v[80:95]
	ds_read_b128 v[220:223], v247 offset:8192
	v_mfma_f32_32x32x16_bf16 v[96:111], v[224:227], v[120:123], v[96:111]
	ds_read_b128 v[224:227], v248
	v_mfma_f32_32x32x16_bf16 v[80:95], v[234:237], v[120:123], v[80:95]
	ds_read_b128 v[234:237], v248 offset:8192
	v_mfma_f32_32x32x16_bf16 v[96:111], v[238:241], v[124:127], v[96:111]
	ds_read_b128 v[238:241], v249
	v_mfma_f32_32x32x16_bf16 v[80:95], v[242:245], v[124:127], v[80:95]
	ds_read_b128 v[242:245], v249 offset:8192
	s_waitcnt lgkmcnt(7)
	v_mfma_f32_32x32x16_bf16 v[96:111], v[208:211], v[128:131], v[96:111]
	v_add_u32_e32 v246, s42, v166
	v_add_u32_e32 v247, s42, v168
	v_add_u32_e32 v248, s42, v169
	v_add_u32_e32 v249, s42, v170
	ds_read_b128 v[208:211], v246
	s_waitcnt lgkmcnt(7)
	v_mfma_f32_32x32x16_bf16 v[80:95], v[212:215], v[128:131], v[80:95]
	ds_read_b128 v[212:215], v246 offset:8192
	s_waitcnt lgkmcnt(7)
	v_mfma_f32_32x32x16_bf16 v[96:111], v[216:219], v[132:135], v[96:111]
	ds_read_b128 v[216:219], v247
	s_waitcnt lgkmcnt(7)
	v_mfma_f32_32x32x16_bf16 v[80:95], v[220:223], v[132:135], v[80:95]
	ds_read_b128 v[220:223], v247 offset:8192
	s_waitcnt lgkmcnt(7)
	v_mfma_f32_32x32x16_bf16 v[96:111], v[224:227], v[136:139], v[96:111]
	ds_read_b128 v[224:227], v248
	s_waitcnt lgkmcnt(7)
	v_mfma_f32_32x32x16_bf16 v[80:95], v[234:237], v[136:139], v[80:95]
	ds_read_b128 v[234:237], v248 offset:8192
	s_waitcnt lgkmcnt(7)
	v_mfma_f32_32x32x16_bf16 v[96:111], v[238:241], v[140:143], v[96:111]
	ds_read_b128 v[238:241], v249
	s_waitcnt lgkmcnt(7)
	v_mfma_f32_32x32x16_bf16 v[80:95], v[242:245], v[140:143], v[80:95]
	ds_read_b128 v[242:245], v249 offset:8192
	s_add_i32 s6, s65, 63
	s_cmp_gt_i32 s6, s44
	s_cbranch_scc1 .Lat_pmasks
	s_cmp_lt_i32 s65, 0x70
	s_cbranch_scc0 .Lat_pnomasks

.Lat_go0:
	s_cmp_gt_i32 s65, s64
	s_cbranch_scc0 .Lat_steady0
	s_add_i32 s6, s65, 0xffffffc0
	s_cmp_gt_i32 s6, s64
	s_cbranch_scc1 .Lat_turn_end0
	s_add_i32 s6, s45, 1
	s_cmp_ge_u32 s6, s46
	s_cbranch_scc1 .Lat_turn_end0
	v_add_u32_e32 v246, s42, v166
	v_add_u32_e32 v247, s42, v168
	v_add_u32_e32 v248, s42, v169
	v_add_u32_e32 v249, s42, v170
	ds_read_b128 v[208:211], v246
	ds_read_b128 v[212:215], v246 offset:8192
	ds_read_b128 v[216:219], v247
	ds_read_b128 v[220:223], v247 offset:8192
	ds_read_b128 v[224:227], v248
	ds_read_b128 v[234:237], v248 offset:8192
	ds_read_b128 v[238:241], v249
	ds_read_b128 v[242:245], v249 offset:8192
	v_add_u32_e32 v246, s42, v251
	v_add_u32_e32 v247, s42, v252
	v_add_u32_e32 v248, s42, v253
	v_add_u32_e32 v249, s42, v254
	s_add_i32 s6, s45, 1
	s_and_b32 s6, s6, 3
	s_lshl_b32 s6, s6, 8
	s_add_i32 s6, s6, 0x10800
	v_add_u32_e32 v152, s6, v164
	ds_read_b128 v[176:179], v152
	ds_read_b128 v[180:183], v152 offset:32
	ds_read_b128 v[192:195], v152 offset:128
	ds_read_b128 v[196:199], v152 offset:160
	ds_read_b128 v[184:187], v152 offset:64
	ds_read_b128 v[188:191], v152 offset:96
	ds_read_b128 v[200:203], v152 offset:192
	ds_read_b128 v[204:207], v152 offset:224
	s_waitcnt lgkmcnt(0)
	v_mfma_f32_32x32x16_bf16 v[176:191], v[208:211], v[112:115], v[176:191]
	ds_read_b128 v[208:211], v246
	v_mfma_f32_32x32x16_bf16 v[192:207], v[212:215], v[112:115], v[192:207]
	ds_read_b128 v[212:215], v246 offset:8192
	v_mfma_f32_32x32x16_bf16 v[176:191], v[216:219], v[116:119], v[176:191]
	ds_read_b128 v[216:219], v247
	v_mfma_f32_32x32x16_bf16 v[192:207], v[220:223], v[116:119], v[192:207]
	ds_read_b128 v[220:223], v247 offset:8192
	v_mfma_f32_32x32x16_bf16 v[176:191], v[224:227], v[120:123], v[176:191]
	ds_read_b128 v[224:227], v248
	v_mfma_f32_32x32x16_bf16 v[192:207], v[234:237], v[120:123], v[192:207]
	ds_read_b128 v[234:237], v248 offset:8192
	v_mfma_f32_32x32x16_bf16 v[176:191], v[238:241], v[124:127], v[176:191]
	ds_read_b128 v[238:241], v249
	v_mfma_f32_32x32x16_bf16 v[192:207], v[242:245], v[124:127], v[192:207]
	ds_read_b128 v[242:245], v249 offset:8192
	s_waitcnt lgkmcnt(7)
	v_mfma_f32_32x32x16_bf16 v[176:191], v[208:211], v[128:131], v[176:191]
	v_add_u32_e32 v246, s43, v166
	v_add_u32_e32 v247, s43, v168
	v_add_u32_e32 v248, s43, v169
	v_add_u32_e32 v249, s43, v170
	ds_read_b128 v[208:211], v246
	s_waitcnt lgkmcnt(7)
	v_mfma_f32_32x32x16_bf16 v[192:207], v[212:215], v[128:131], v[192:207]
	ds_read_b128 v[212:215], v246 offset:8192
	s_waitcnt lgkmcnt(7)
	v_mfma_f32_32x32x16_bf16 v[176:191], v[216:219], v[132:135], v[176:191]
	ds_read_b128 v[216:219], v247
	s_waitcnt lgkmcnt(7)
	v_mfma_f32_32x32x16_bf16 v[192:207], v[220:223], v[132:135], v[192:207]
	ds_read_b128 v[220:223], v247 offset:8192
	s_waitcnt lgkmcnt(7)
	v_mfma_f32_32x32x16_bf16 v[176:191], v[224:227], v[136:139], v[176:191]
	ds_read_b128 v[224:227], v248
	s_waitcnt lgkmcnt(7)
	v_mfma_f32_32x32x16_bf16 v[192:207], v[234:237], v[136:139], v[192:207]
	ds_read_b128 v[234:237], v248 offset:8192
	s_waitcnt lgkmcnt(7)
	v_mfma_f32_32x32x16_bf16 v[176:191], v[238:241], v[140:143], v[176:191]
	ds_read_b128 v[238:241], v249
	s_waitcnt lgkmcnt(7)
	v_mfma_f32_32x32x16_bf16 v[192:207], v[242:245], v[140:143], v[192:207]
	ds_read_b128 v[242:245], v249 offset:8192
	s_add_i32 s6, s65, -1
	s_cmp_gt_i32 s6, s44
	s_cbranch_scc1 .Lat_pmask0
	s_cmp_lt_i32 s65, 0xb0
	s_cbranch_scc0 .Lat_pnomask0

.Lat_steady0:
	s_waitcnt lgkmcnt(0)
	v_add_u32_e32 v246, s42, v251
	v_add_u32_e32 v247, s42, v252
	v_add_u32_e32 v248, s42, v253
	v_add_u32_e32 v249, s42, v254
	v_add_u32_e32 v153, s66, v162
	v_mfma_f32_32x32x16_bf16 v[176:191], v[208:211], v[112:115], v[176:191]
	ds_read_b128 v[208:211], v246
	v_exp_f32_e32 v80, v80
	v_exp_f32_e32 v81, v81
	v_add_f32_e32 v148, v96, v100
	v_add_f32_e32 v149, v97, v101
	v_mfma_f32_32x32x16_bf16 v[192:207], v[212:215], v[112:115], v[192:207]
	ds_read_b128 v[212:215], v246 offset:8192
	v_exp_f32_e32 v82, v82
	v_exp_f32_e32 v83, v83
	v_add_f32_e32 v150, v98, v102
	v_add_f32_e32 v151, v99, v103
	v_mfma_f32_32x32x16_bf16 v[176:191], v[216:219], v[116:119], v[176:191]
	ds_read_b128 v[216:219], v247
	v_exp_f32_e32 v84, v84
	v_exp_f32_e32 v85, v85
	v_add_f32_e32 v148, v148, v104
	v_add_f32_e32 v149, v149, v105
	v_mfma_f32_32x32x16_bf16 v[192:207], v[220:223], v[116:119], v[192:207]
	ds_read_b128 v[220:223], v247 offset:8192
	v_exp_f32_e32 v86, v86
	v_exp_f32_e32 v87, v87
	v_add_f32_e32 v150, v150, v106
	v_add_f32_e32 v151, v151, v107
	v_mfma_f32_32x32x16_bf16 v[176:191], v[224:227], v[120:123], v[176:191]
	ds_read_b128 v[224:227], v248
	v_exp_f32_e32 v88, v88
	v_exp_f32_e32 v89, v89
	v_add_f32_e32 v148, v148, v108
	v_add_f32_e32 v149, v149, v109
	v_mfma_f32_32x32x16_bf16 v[192:207], v[234:237], v[120:123], v[192:207]
	ds_read_b128 v[234:237], v248 offset:8192
	v_exp_f32_e32 v90, v90
	v_exp_f32_e32 v91, v91
	v_add_f32_e32 v150, v150, v110
	v_add_f32_e32 v151, v151, v111
	v_mfma_f32_32x32x16_bf16 v[176:191], v[238:241], v[124:127], v[176:191]
	ds_read_b128 v[238:241], v249
	v_exp_f32_e32 v92, v92
	v_exp_f32_e32 v93, v93
	v_add_f32_e32 v148, v148, v80
	v_add_f32_e32 v149, v149, v81
	v_mfma_f32_32x32x16_bf16 v[192:207], v[242:245], v[124:127], v[192:207]
	ds_read_b128 v[242:245], v249 offset:8192
	v_exp_f32_e32 v94, v94
	v_exp_f32_e32 v95, v95
	v_add_f32_e32 v150, v150, v82
	v_add_f32_e32 v151, v151, v83
	s_waitcnt lgkmcnt(7)
	v_mfma_f32_32x32x16_bf16 v[176:191], v[208:211], v[128:131], v[176:191]
	ds_read_b64_tr_b16 v[208:209], v153 offset:0
	ds_read_b64_tr_b16 v[210:211], v153 offset:2048
	v_add_f32_e32 v148, v148, v84
	v_add_f32_e32 v149, v149, v85
	v_add_f32_e32 v150, v150, v86
	v_add_f32_e32 v151, v151, v87
	v_add_f32_e32 v148, v148, v88
	v_add_f32_e32 v149, v149, v89
	s_waitcnt lgkmcnt(8)
	v_mfma_f32_32x32x16_bf16 v[192:207], v[212:215], v[128:131], v[192:207]
	ds_read_b64_tr_b16 v[212:213], v153 offset:512
	ds_read_b64_tr_b16 v[214:215], v153 offset:2560
	v_add_f32_e32 v150, v150, v90
	v_add_f32_e32 v151, v151, v91
	v_add_f32_e32 v148, v148, v92
	v_add_f32_e32 v149, v149, v93
	v_add_f32_e32 v150, v150, v94
	v_add_f32_e32 v151, v151, v95
	s_waitcnt lgkmcnt(9)
	v_mfma_f32_32x32x16_bf16 v[176:191], v[216:219], v[132:135], v[176:191]
	ds_read_b64_tr_b16 v[216:217], v153 offset:1024
	ds_read_b64_tr_b16 v[218:219], v153 offset:3072
	v_add_f32_e32 v148, v148, v149
	v_add_f32_e32 v150, v150, v151
	v_add_f32_e32 v148, v148, v150
	v_mov_b32_e32 v152, v148
	v_cvt_pk_bf16_f32 v96, v96, v97
	v_cvt_pk_bf16_f32 v97, v98, v99
	s_waitcnt lgkmcnt(10)
	v_mfma_f32_32x32x16_bf16 v[192:207], v[220:223], v[132:135], v[192:207]
	ds_read_b64_tr_b16 v[220:221], v153 offset:1536
	ds_read_b64_tr_b16 v[222:223], v153 offset:3584
	v_permlane32_swap_b32_e32 v148, v152
	v_cvt_pk_bf16_f32 v98, v100, v101
	v_cvt_pk_bf16_f32 v99, v102, v103
	v_add_f32_e32 v148, v148, v152
	v_cvt_pk_bf16_f32 v100, v104, v105
	v_cvt_pk_bf16_f32 v101, v106, v107
	s_waitcnt lgkmcnt(11)
	v_mfma_f32_32x32x16_bf16 v[176:191], v[224:227], v[136:139], v[176:191]
	ds_read_b64_tr_b16 v[224:225], v153 offset:4096
	ds_read_b64_tr_b16 v[226:227], v153 offset:6144
	v_cvt_pk_bf16_f32 v102, v108, v109
	v_cvt_pk_bf16_f32 v103, v110, v111
	v_cvt_pk_bf16_f32 v104, v80, v81
	v_cvt_pk_bf16_f32 v105, v82, v83
	v_cvt_pk_bf16_f32 v106, v84, v85
	v_cvt_pk_bf16_f32 v107, v86, v87
	s_waitcnt lgkmcnt(12)
	v_mfma_f32_32x32x16_bf16 v[192:207], v[234:237], v[136:139], v[192:207]
	ds_read_b64_tr_b16 v[234:235], v153 offset:4608
	ds_read_b64_tr_b16 v[236:237], v153 offset:6656
	v_cvt_pk_bf16_f32 v108, v88, v89
	v_cvt_pk_bf16_f32 v109, v90, v91
	v_cvt_pk_bf16_f32 v110, v92, v93
	v_cvt_pk_bf16_f32 v111, v94, v95
	v_fma_f32 v174, v174, v233, v148
	s_nop 0
	s_waitcnt lgkmcnt(13)
	v_mfma_f32_32x32x16_bf16 v[176:191], v[238:241], v[140:143], v[176:191]
	ds_read_b64_tr_b16 v[238:239], v153 offset:5120
	ds_read_b64_tr_b16 v[240:241], v153 offset:7168
	v_permlane32_swap_b32_e32 v96, v98
	v_permlane32_swap_b32_e32 v97, v99
	v_permlane32_swap_b32_e32 v100, v102
	v_permlane32_swap_b32_e32 v101, v103
	v_permlane32_swap_b32_e32 v104, v106
	v_permlane32_swap_b32_e32 v105, v107
	s_waitcnt lgkmcnt(14)
	v_mfma_f32_32x32x16_bf16 v[192:207], v[242:245], v[140:143], v[192:207]
	ds_read_b64_tr_b16 v[242:243], v153 offset:5632
	ds_read_b64_tr_b16 v[244:245], v153 offset:7680
	v_permlane32_swap_b32_e32 v108, v110
	v_permlane32_swap_b32_e32 v109, v111
	s_add_i32 s6, s65, -1
	s_cmp_gt_i32 s6, s44
	s_cbranch_scc1 .Lat_mask0
	s_cmp_lt_i32 s65, 0xb0
	s_cbranch_scc0 .Lat_nomask0

.Lat_norescale0:
	v_add_u32_e32 v246, s43, v166
	v_add_u32_e32 v247, s43, v168
	v_add_u32_e32 v248, s43, v169
	v_add_u32_e32 v249, s43, v170
	s_add_i32 s6, s45, 2
	s_and_b32 s6, s6, 3
	s_lshl_b32 s6, s6, 8
	s_add_i32 s6, s6, 0x10800
	v_add_u32_e32 v152, s6, v164
	s_add_i32 s6, s45, 1
	s_cmp_ge_u32 s6, s46
	s_cbranch_scc1 .Lat_p2last0
	s_waitcnt lgkmcnt(14)
	v_mfma_f32_32x32x16_bf16 v[64:79], v[96:99], v[208:211], v[64:79]
	ds_read_b64_tr_b16 v[208:209], v153 offset:8192
	ds_read_b64_tr_b16 v[210:211], v153 offset:10240
	ds_read_b128 v[80:83], v152 offset:128
	s_waitcnt lgkmcnt(15)
	v_mfma_f32_32x32x16_bf16 v[48:63], v[96:99], v[212:215], v[48:63]
	ds_read_b64_tr_b16 v[212:213], v153 offset:8704
	ds_read_b64_tr_b16 v[214:215], v153 offset:10752
	ds_read_b128 v[84:87], v152 offset:160
	v_max3_f32 v0, v176, v177, v178
	v_max3_f32 v2, v184, v185, v186
	v_max3_f32 v3, v192, v193, v194
	v_max3_f32 v4, v200, v201, v202
	v_max3_f32 v0, v0, v179, v180
	v_max3_f32 v2, v2, v187, v188
	s_waitcnt lgkmcnt(15)
	v_mfma_f32_32x32x16_bf16 v[32:47], v[96:99], v[216:219], v[32:47]
	ds_read_b64_tr_b16 v[216:217], v153 offset:9216
	ds_read_b64_tr_b16 v[218:219], v153 offset:11264
	ds_read_b128 v[88:91], v152 offset:192
	v_max3_f32 v3, v3, v195, v196
	v_max3_f32 v4, v4, v203, v204
	v_max3_f32 v0, v0, v181, v182
	v_max3_f32 v2, v2, v189, v190
	v_max3_f32 v3, v3, v197, v198
	v_max3_f32 v4, v4, v205, v206
	s_waitcnt lgkmcnt(15)
	v_mfma_f32_32x32x16_bf16 v[16:31], v[96:99], v[220:223], v[16:31]
	ds_read_b64_tr_b16 v[220:221], v153 offset:9728
	ds_read_b64_tr_b16 v[222:223], v153 offset:11776
	ds_read_b128 v[92:95], v152 offset:224
	ds_read_b128 v[96:99], v152
	v_max_f32_e32 v0, v0, v183
	v_max_f32_e32 v2, v2, v191
	v_max_f32_e32 v3, v3, v199
	v_max_f32_e32 v4, v4, v207
	v_max3_f32 v0, v0, v2, v3
	v_max_f32_e32 v0, v0, v4
	s_waitcnt lgkmcnt(15)
	v_mfma_f32_32x32x16_bf16 v[64:79], v[100:103], v[224:227], v[64:79]
	ds_read_b64_tr_b16 v[224:225], v153 offset:12288
	ds_read_b64_tr_b16 v[226:227], v153 offset:14336
	v_mov_b32_e32 v2, v0
	s_nop 1
	v_permlane32_swap_b32_e32 v0, v2
	v_max_f32_e32 v2, v2, v2
	v_max_f32_e32 v0, v0, v0
	s_waitcnt lgkmcnt(15)
	v_mfma_f32_32x32x16_bf16 v[48:63], v[100:103], v[234:237], v[48:63]
	ds_read_b64_tr_b16 v[234:235], v153 offset:12800
	ds_read_b64_tr_b16 v[236:237], v153 offset:14848
	v_max_f32_e32 v0, v0, v2
	v_sub_f32_e32 v2, v0, v173
	v_mul_f32_e32 v2, 0x3db504f3, v2
	v_cmp_ge_f32_e32 vcc, s63, v2
	v_max_f32_e32 v2, v173, v173
	v_max_f32_e32 v2, v2, v0
	s_waitcnt lgkmcnt(15)
	v_mfma_f32_32x32x16_bf16 v[32:47], v[100:103], v[238:241], v[32:47]
	ds_read_b64_tr_b16 v[238:239], v153 offset:13312
	ds_read_b64_tr_b16 v[240:241], v153 offset:15360
	v_sub_f32_e32 v0, v173, v2
	v_mul_f32_e32 v0, 0x3e0293ee, v0
	v_exp_f32_e32 v0, v0
	s_cmp_eq_u64 vcc, exec
	s_cselect_b64 s[6:7], -1, 0
	v_cndmask_b32_e64 v0, v0, 1.0, s[6:7]
	s_waitcnt lgkmcnt(15)
	v_mfma_f32_32x32x16_bf16 v[16:31], v[100:103], v[242:245], v[16:31]
	ds_read_b64_tr_b16 v[242:243], v153 offset:13824
	ds_read_b64_tr_b16 v[244:245], v153 offset:15872
	ds_read_b128 v[100:103], v152 offset:32
	v_cmp_gt_f32_e32 vcc, 1.0, v0
	v_mov_b32_e32 v233, v0
	v_cndmask_b32_e64 v173, v2, v173, s[6:7]
	s_cmp_lg_u64 vcc, 0
	s_cselect_b32 s99, 1, 0
	v_mul_f32_e32 v2, 0xbe0293ee, v173
	v_fmamk_f32 v176, v176, 0x3e0293ee, v2
	s_waitcnt lgkmcnt(15)
	v_mfma_f32_32x32x16_bf16 v[64:79], v[104:107], v[208:211], v[64:79]
	ds_read_b128 v[208:211], v246
	v_fmamk_f32 v177, v177, 0x3e0293ee, v2
	v_fmamk_f32 v178, v178, 0x3e0293ee, v2
	v_fmamk_f32 v179, v179, 0x3e0293ee, v2
	v_fmamk_f32 v180, v180, 0x3e0293ee, v2
	v_fmamk_f32 v181, v181, 0x3e0293ee, v2
	v_fmamk_f32 v182, v182, 0x3e0293ee, v2
	s_waitcnt lgkmcnt(15)
	v_mfma_f32_32x32x16_bf16 v[48:63], v[104:107], v[212:215], v[48:63]
	ds_read_b128 v[212:215], v246 offset:8192
	v_fmamk_f32 v183, v183, 0x3e0293ee, v2
	v_fmamk_f32 v184, v184, 0x3e0293ee, v2
	v_fmamk_f32 v185, v185, 0x3e0293ee, v2
	v_fmamk_f32 v186, v186, 0x3e0293ee, v2
	v_fmamk_f32 v187, v187, 0x3e0293ee, v2
	v_fmamk_f32 v188, v188, 0x3e0293ee, v2
	s_waitcnt lgkmcnt(15)
	v_mfma_f32_32x32x16_bf16 v[32:47], v[104:107], v[216:219], v[32:47]
	ds_read_b128 v[216:219], v247
	v_fmamk_f32 v189, v189, 0x3e0293ee, v2
	v_fmamk_f32 v190, v190, 0x3e0293ee, v2
	v_fmamk_f32 v191, v191, 0x3e0293ee, v2
	v_exp_f32_e32 v176, v176
	v_fmamk_f32 v192, v192, 0x3e0293ee, v2
	s_waitcnt lgkmcnt(14)
	v_mfma_f32_32x32x16_bf16 v[16:31], v[104:107], v[220:223], v[16:31]
	ds_read_b128 v[220:223], v247 offset:8192
	ds_read_b128 v[104:107], v152 offset:64
	v_exp_f32_e32 v177, v177
	v_fmamk_f32 v193, v193, 0x3e0293ee, v2
	v_exp_f32_e32 v178, v178
	v_fmamk_f32 v194, v194, 0x3e0293ee, v2
	s_waitcnt lgkmcnt(12)
	v_mfma_f32_32x32x16_bf16 v[64:79], v[108:111], v[224:227], v[64:79]
	ds_read_b128 v[224:227], v248
	v_exp_f32_e32 v179, v179
	v_fmamk_f32 v195, v195, 0x3e0293ee, v2
	v_exp_f32_e32 v180, v180
	v_fmamk_f32 v196, v196, 0x3e0293ee, v2
	s_waitcnt lgkmcnt(11)
	v_mfma_f32_32x32x16_bf16 v[48:63], v[108:111], v[234:237], v[48:63]
	ds_read_b128 v[234:237], v248 offset:8192
	v_exp_f32_e32 v181, v181
	v_fmamk_f32 v197, v197, 0x3e0293ee, v2
	v_exp_f32_e32 v182, v182
	v_fmamk_f32 v198, v198, 0x3e0293ee, v2
	s_waitcnt lgkmcnt(10)
	v_mfma_f32_32x32x16_bf16 v[32:47], v[108:111], v[238:241], v[32:47]
	ds_read_b128 v[238:241], v249
	v_exp_f32_e32 v183, v183
	v_fmamk_f32 v199, v199, 0x3e0293ee, v2
	v_exp_f32_e32 v184, v184
	v_fmamk_f32 v200, v200, 0x3e0293ee, v2
	s_waitcnt lgkmcnt(9)
	v_mfma_f32_32x32x16_bf16 v[16:31], v[108:111], v[242:245], v[16:31]
	ds_read_b128 v[242:245], v249 offset:8192
	ds_read_b128 v[108:111], v152 offset:96
	v_exp_f32_e32 v185, v185
	v_fmamk_f32 v201, v201, 0x3e0293ee, v2
	v_exp_f32_e32 v186, v186
	v_fmamk_f32 v202, v202, 0x3e0293ee, v2
	v_exp_f32_e32 v187, v187
	v_fmamk_f32 v203, v203, 0x3e0293ee, v2
	v_exp_f32_e32 v188, v188
	v_fmamk_f32 v204, v204, 0x3e0293ee, v2
	v_exp_f32_e32 v189, v189
	v_fmamk_f32 v205, v205, 0x3e0293ee, v2
	v_exp_f32_e32 v190, v190
	v_fmamk_f32 v206, v206, 0x3e0293ee, v2
	v_exp_f32_e32 v191, v191
	v_fmamk_f32 v207, v207, 0x3e0293ee, v2
	s_branch .Lat_turn_end0

.Lat_go1:
	s_cmp_gt_i32 s65, s64
	s_cbranch_scc0 .Lat_steady1
	s_add_i32 s6, s65, 0xffffffc0
	s_cmp_gt_i32 s6, s64
	s_cbranch_scc1 .Lat_turn_end1
	s_add_i32 s6, s45, 1
	s_cmp_ge_u32 s6, s46
	s_cbranch_scc1 .Lat_turn_end1
	v_add_u32_e32 v246, s42, v166
	v_add_u32_e32 v247, s42, v168
	v_add_u32_e32 v248, s42, v169
	v_add_u32_e32 v249, s42, v170
	ds_read_b128 v[208:211], v246
	ds_read_b128 v[212:215], v246 offset:8192
	ds_read_b128 v[216:219], v247
	ds_read_b128 v[220:223], v247 offset:8192
	ds_read_b128 v[224:227], v248
	ds_read_b128 v[234:237], v248 offset:8192
	ds_read_b128 v[238:241], v249
	ds_read_b128 v[242:245], v249 offset:8192
	v_add_u32_e32 v246, s42, v251
	v_add_u32_e32 v247, s42, v252
	v_add_u32_e32 v248, s42, v253
	v_add_u32_e32 v249, s42, v254
	s_add_i32 s6, s45, 1
	s_and_b32 s6, s6, 3
	s_lshl_b32 s6, s6, 8
	s_add_i32 s6, s6, 0x10800
	v_add_u32_e32 v152, s6, v164
	ds_read_b128 v[96:99], v152
	ds_read_b128 v[100:103], v152 offset:32
	ds_read_b128 v[80:83], v152 offset:128
	ds_read_b128 v[84:87], v152 offset:160
	ds_read_b128 v[104:107], v152 offset:64
	ds_read_b128 v[108:111], v152 offset:96
	ds_read_b128 v[88:91], v152 offset:192
	ds_read_b128 v[92:95], v152 offset:224
	s_waitcnt lgkmcnt(0)
	v_mfma_f32_32x32x16_bf16 v[96:111], v[208:211], v[112:115], v[96:111]
	ds_read_b128 v[208:211], v246
	v_mfma_f32_32x32x16_bf16 v[80:95], v[212:215], v[112:115], v[80:95]
	ds_read_b128 v[212:215], v246 offset:8192
	v_mfma_f32_32x32x16_bf16 v[96:111], v[216:219], v[116:119], v[96:111]
	ds_read_b128 v[216:219], v247
	v_mfma_f32_32x32x16_bf16 v[80:95], v[220:223], v[116:119], v[80:95]
	ds_read_b128 v[220:223], v247 offset:8192
	v_mfma_f32_32x32x16_bf16 v[96:111], v[224:227], v[120:123], v[96:111]
	ds_read_b128 v[224:227], v248
	v_mfma_f32_32x32x16_bf16 v[80:95], v[234:237], v[120:123], v[80:95]
	ds_read_b128 v[234:237], v248 offset:8192
	v_mfma_f32_32x32x16_bf16 v[96:111], v[238:241], v[124:127], v[96:111]
	ds_read_b128 v[238:241], v249
	v_mfma_f32_32x32x16_bf16 v[80:95], v[242:245], v[124:127], v[80:95]
	ds_read_b128 v[242:245], v249 offset:8192
	s_waitcnt lgkmcnt(7)
	v_mfma_f32_32x32x16_bf16 v[96:111], v[208:211], v[128:131], v[96:111]
	v_add_u32_e32 v246, s43, v166
	v_add_u32_e32 v247, s43, v168
	v_add_u32_e32 v248, s43, v169
	v_add_u32_e32 v249, s43, v170
	ds_read_b128 v[208:211], v246
	s_waitcnt lgkmcnt(7)
	v_mfma_f32_32x32x16_bf16 v[80:95], v[212:215], v[128:131], v[80:95]
	ds_read_b128 v[212:215], v246 offset:8192
	s_waitcnt lgkmcnt(7)
	v_mfma_f32_32x32x16_bf16 v[96:111], v[216:219], v[132:135], v[96:111]
	ds_read_b128 v[216:219], v247
	s_waitcnt lgkmcnt(7)
	v_mfma_f32_32x32x16_bf16 v[80:95], v[220:223], v[132:135], v[80:95]
	ds_read_b128 v[220:223], v247 offset:8192
	s_waitcnt lgkmcnt(7)
	v_mfma_f32_32x32x16_bf16 v[96:111], v[224:227], v[136:139], v[96:111]
	ds_read_b128 v[224:227], v248
	s_waitcnt lgkmcnt(7)
	v_mfma_f32_32x32x16_bf16 v[80:95], v[234:237], v[136:139], v[80:95]
	ds_read_b128 v[234:237], v248 offset:8192
	s_waitcnt lgkmcnt(7)
	v_mfma_f32_32x32x16_bf16 v[96:111], v[238:241], v[140:143], v[96:111]
	ds_read_b128 v[238:241], v249
	s_waitcnt lgkmcnt(7)
	v_mfma_f32_32x32x16_bf16 v[80:95], v[242:245], v[140:143], v[80:95]
	ds_read_b128 v[242:245], v249 offset:8192
	s_add_i32 s6, s65, -1
	s_cmp_gt_i32 s6, s44
	s_cbranch_scc1 .Lat_pmask1
	s_cmp_lt_i32 s65, 0xb0
	s_cbranch_scc0 .Lat_pnomask1

.Lat_steady1:
	s_waitcnt lgkmcnt(0)
	v_add_u32_e32 v246, s42, v251
	v_add_u32_e32 v247, s42, v252
	v_add_u32_e32 v248, s42, v253
	v_add_u32_e32 v249, s42, v254
	v_add_u32_e32 v153, s66, v162
	v_mfma_f32_32x32x16_bf16 v[96:111], v[208:211], v[112:115], v[96:111]
	ds_read_b128 v[208:211], v246
	v_exp_f32_e32 v192, v192
	v_exp_f32_e32 v193, v193
	v_add_f32_e32 v148, v176, v180
	v_add_f32_e32 v149, v177, v181
	v_mfma_f32_32x32x16_bf16 v[80:95], v[212:215], v[112:115], v[80:95]
	ds_read_b128 v[212:215], v246 offset:8192
	v_exp_f32_e32 v194, v194
	v_exp_f32_e32 v195, v195
	v_add_f32_e32 v150, v178, v182
	v_add_f32_e32 v151, v179, v183
	v_mfma_f32_32x32x16_bf16 v[96:111], v[216:219], v[116:119], v[96:111]
	ds_read_b128 v[216:219], v247
	v_exp_f32_e32 v196, v196
	v_exp_f32_e32 v197, v197
	v_add_f32_e32 v148, v148, v184
	v_add_f32_e32 v149, v149, v185
	v_mfma_f32_32x32x16_bf16 v[80:95], v[220:223], v[116:119], v[80:95]
	ds_read_b128 v[220:223], v247 offset:8192
	v_exp_f32_e32 v198, v198
	v_exp_f32_e32 v199, v199
	v_add_f32_e32 v150, v150, v186
	v_add_f32_e32 v151, v151, v187
	v_mfma_f32_32x32x16_bf16 v[96:111], v[224:227], v[120:123], v[96:111]
	ds_read_b128 v[224:227], v248
	v_exp_f32_e32 v200, v200
	v_exp_f32_e32 v201, v201
	v_add_f32_e32 v148, v148, v188
	v_add_f32_e32 v149, v149, v189
	v_mfma_f32_32x32x16_bf16 v[80:95], v[234:237], v[120:123], v[80:95]
	ds_read_b128 v[234:237], v248 offset:8192
	v_exp_f32_e32 v202, v202
	v_exp_f32_e32 v203, v203
	v_add_f32_e32 v150, v150, v190
	v_add_f32_e32 v151, v151, v191
	v_mfma_f32_32x32x16_bf16 v[96:111], v[238:241], v[124:127], v[96:111]
	ds_read_b128 v[238:241], v249
	v_exp_f32_e32 v204, v204
	v_exp_f32_e32 v205, v205
	v_add_f32_e32 v148, v148, v192
	v_add_f32_e32 v149, v149, v193
	v_mfma_f32_32x32x16_bf16 v[80:95], v[242:245], v[124:127], v[80:95]
	ds_read_b128 v[242:245], v249 offset:8192
	v_exp_f32_e32 v206, v206
	v_exp_f32_e32 v207, v207
	v_add_f32_e32 v150, v150, v194
	v_add_f32_e32 v151, v151, v195
	s_waitcnt lgkmcnt(7)
	v_mfma_f32_32x32x16_bf16 v[96:111], v[208:211], v[128:131], v[96:111]
	ds_read_b64_tr_b16 v[208:209], v153 offset:0
	ds_read_b64_tr_b16 v[210:211], v153 offset:2048
	v_add_f32_e32 v148, v148, v196
	v_add_f32_e32 v149, v149, v197
	v_add_f32_e32 v150, v150, v198
	v_add_f32_e32 v151, v151, v199
	v_add_f32_e32 v148, v148, v200
	v_add_f32_e32 v149, v149, v201
	s_waitcnt lgkmcnt(8)
	v_mfma_f32_32x32x16_bf16 v[80:95], v[212:215], v[128:131], v[80:95]
	ds_read_b64_tr_b16 v[212:213], v153 offset:512
	ds_read_b64_tr_b16 v[214:215], v153 offset:2560
	v_add_f32_e32 v150, v150, v202
	v_add_f32_e32 v151, v151, v203
	v_add_f32_e32 v148, v148, v204
	v_add_f32_e32 v149, v149, v205
	v_add_f32_e32 v150, v150, v206
	v_add_f32_e32 v151, v151, v207
	s_waitcnt lgkmcnt(9)
	v_mfma_f32_32x32x16_bf16 v[96:111], v[216:219], v[132:135], v[96:111]
	ds_read_b64_tr_b16 v[216:217], v153 offset:1024
	ds_read_b64_tr_b16 v[218:219], v153 offset:3072
	v_add_f32_e32 v148, v148, v149
	v_add_f32_e32 v150, v150, v151
	v_add_f32_e32 v148, v148, v150
	v_mov_b32_e32 v152, v148
	v_cvt_pk_bf16_f32 v176, v176, v177
	v_cvt_pk_bf16_f32 v177, v178, v179
	s_waitcnt lgkmcnt(10)
	v_mfma_f32_32x32x16_bf16 v[80:95], v[220:223], v[132:135], v[80:95]
	ds_read_b64_tr_b16 v[220:221], v153 offset:1536
	ds_read_b64_tr_b16 v[222:223], v153 offset:3584
	v_permlane32_swap_b32_e32 v148, v152
	v_cvt_pk_bf16_f32 v178, v180, v181
	v_cvt_pk_bf16_f32 v179, v182, v183
	v_add_f32_e32 v148, v148, v152
	v_cvt_pk_bf16_f32 v180, v184, v185
	v_cvt_pk_bf16_f32 v181, v186, v187
	s_waitcnt lgkmcnt(11)
	v_mfma_f32_32x32x16_bf16 v[96:111], v[224:227], v[136:139], v[96:111]
	ds_read_b64_tr_b16 v[224:225], v153 offset:4096
	ds_read_b64_tr_b16 v[226:227], v153 offset:6144
	v_cvt_pk_bf16_f32 v182, v188, v189
	v_cvt_pk_bf16_f32 v183, v190, v191
	v_cvt_pk_bf16_f32 v184, v192, v193
	v_cvt_pk_bf16_f32 v185, v194, v195
	v_cvt_pk_bf16_f32 v186, v196, v197
	v_cvt_pk_bf16_f32 v187, v198, v199
	s_waitcnt lgkmcnt(12)
	v_mfma_f32_32x32x16_bf16 v[80:95], v[234:237], v[136:139], v[80:95]
	ds_read_b64_tr_b16 v[234:235], v153 offset:4608
	ds_read_b64_tr_b16 v[236:237], v153 offset:6656
	v_cvt_pk_bf16_f32 v188, v200, v201
	v_cvt_pk_bf16_f32 v189, v202, v203
	v_cvt_pk_bf16_f32 v190, v204, v205
	v_cvt_pk_bf16_f32 v191, v206, v207
	v_fma_f32 v174, v174, v233, v148
	s_nop 0
	s_waitcnt lgkmcnt(13)
	v_mfma_f32_32x32x16_bf16 v[96:111], v[238:241], v[140:143], v[96:111]
	ds_read_b64_tr_b16 v[238:239], v153 offset:5120
	ds_read_b64_tr_b16 v[240:241], v153 offset:7168
	v_permlane32_swap_b32_e32 v176, v178
	v_permlane32_swap_b32_e32 v177, v179
	v_permlane32_swap_b32_e32 v180, v182
	v_permlane32_swap_b32_e32 v181, v183
	v_permlane32_swap_b32_e32 v184, v186
	v_permlane32_swap_b32_e32 v185, v187
	s_waitcnt lgkmcnt(14)
	v_mfma_f32_32x32x16_bf16 v[80:95], v[242:245], v[140:143], v[80:95]
	ds_read_b64_tr_b16 v[242:243], v153 offset:5632
	ds_read_b64_tr_b16 v[244:245], v153 offset:7680
	v_permlane32_swap_b32_e32 v188, v190
	v_permlane32_swap_b32_e32 v189, v191
	s_add_i32 s6, s65, -1
	s_cmp_gt_i32 s6, s44
	s_cbranch_scc1 .Lat_mask1
	s_cmp_lt_i32 s65, 0xb0
	s_cbranch_scc0 .Lat_nomask1

.Lat_norescale1:
	v_add_u32_e32 v246, s43, v166
	v_add_u32_e32 v247, s43, v168
	v_add_u32_e32 v248, s43, v169
	v_add_u32_e32 v249, s43, v170
	s_add_i32 s6, s45, 2
	s_and_b32 s6, s6, 3
	s_lshl_b32 s6, s6, 8
	s_add_i32 s6, s6, 0x10800
	v_add_u32_e32 v152, s6, v164
	s_add_i32 s6, s45, 1
	s_cmp_ge_u32 s6, s46
	s_cbranch_scc1 .Lat_p2last1
	s_waitcnt lgkmcnt(14)
	v_mfma_f32_32x32x16_bf16 v[64:79], v[176:179], v[208:211], v[64:79]
	ds_read_b64_tr_b16 v[208:209], v153 offset:8192
	ds_read_b64_tr_b16 v[210:211], v153 offset:10240
	ds_read_b128 v[192:195], v152 offset:128
	s_waitcnt lgkmcnt(15)
	v_mfma_f32_32x32x16_bf16 v[48:63], v[176:179], v[212:215], v[48:63]
	ds_read_b64_tr_b16 v[212:213], v153 offset:8704
	ds_read_b64_tr_b16 v[214:215], v153 offset:10752
	ds_read_b128 v[196:199], v152 offset:160
	v_max3_f32 v0, v96, v97, v98
	v_max3_f32 v2, v104, v105, v106
	v_max3_f32 v3, v80, v81, v82
	v_max3_f32 v4, v88, v89, v90
	v_max3_f32 v0, v0, v99, v100
	v_max3_f32 v2, v2, v107, v108
	s_waitcnt lgkmcnt(15)
	v_mfma_f32_32x32x16_bf16 v[32:47], v[176:179], v[216:219], v[32:47]
	ds_read_b64_tr_b16 v[216:217], v153 offset:9216
	ds_read_b64_tr_b16 v[218:219], v153 offset:11264
	ds_read_b128 v[200:203], v152 offset:192
	v_max3_f32 v3, v3, v83, v84
	v_max3_f32 v4, v4, v91, v92
	v_max3_f32 v0, v0, v101, v102
	v_max3_f32 v2, v2, v109, v110
	v_max3_f32 v3, v3, v85, v86
	v_max3_f32 v4, v4, v93, v94
	s_waitcnt lgkmcnt(15)
	v_mfma_f32_32x32x16_bf16 v[16:31], v[176:179], v[220:223], v[16:31]
	ds_read_b64_tr_b16 v[220:221], v153 offset:9728
	ds_read_b64_tr_b16 v[222:223], v153 offset:11776
	ds_read_b128 v[204:207], v152 offset:224
	ds_read_b128 v[176:179], v152
	v_max_f32_e32 v0, v0, v103
	v_max_f32_e32 v2, v2, v111
	v_max_f32_e32 v3, v3, v87
	v_max_f32_e32 v4, v4, v95
	v_max3_f32 v0, v0, v2, v3
	v_max_f32_e32 v0, v0, v4
	s_waitcnt lgkmcnt(15)
	v_mfma_f32_32x32x16_bf16 v[64:79], v[180:183], v[224:227], v[64:79]
	ds_read_b64_tr_b16 v[224:225], v153 offset:12288
	ds_read_b64_tr_b16 v[226:227], v153 offset:14336
	v_mov_b32_e32 v2, v0
	s_nop 1
	v_permlane32_swap_b32_e32 v0, v2
	v_max_f32_e32 v2, v2, v2
	v_max_f32_e32 v0, v0, v0
	s_waitcnt lgkmcnt(15)
	v_mfma_f32_32x32x16_bf16 v[48:63], v[180:183], v[234:237], v[48:63]
	ds_read_b64_tr_b16 v[234:235], v153 offset:12800
	ds_read_b64_tr_b16 v[236:237], v153 offset:14848
	v_max_f32_e32 v0, v0, v2
	v_sub_f32_e32 v2, v0, v173
	v_mul_f32_e32 v2, 0x3db504f3, v2
	v_cmp_ge_f32_e32 vcc, s63, v2
	v_max_f32_e32 v2, v173, v173
	v_max_f32_e32 v2, v2, v0
	s_waitcnt lgkmcnt(15)
	v_mfma_f32_32x32x16_bf16 v[32:47], v[180:183], v[238:241], v[32:47]
	ds_read_b64_tr_b16 v[238:239], v153 offset:13312
	ds_read_b64_tr_b16 v[240:241], v153 offset:15360
	v_sub_f32_e32 v0, v173, v2
	v_mul_f32_e32 v0, 0x3e0293ee, v0
	v_exp_f32_e32 v0, v0
	s_cmp_eq_u64 vcc, exec
	s_cselect_b64 s[6:7], -1, 0
	v_cndmask_b32_e64 v0, v0, 1.0, s[6:7]
	s_waitcnt lgkmcnt(15)
	v_mfma_f32_32x32x16_bf16 v[16:31], v[180:183], v[242:245], v[16:31]
	ds_read_b64_tr_b16 v[242:243], v153 offset:13824
	ds_read_b64_tr_b16 v[244:245], v153 offset:15872
	ds_read_b128 v[180:183], v152 offset:32
	v_cmp_gt_f32_e32 vcc, 1.0, v0
	v_mov_b32_e32 v233, v0
	v_cndmask_b32_e64 v173, v2, v173, s[6:7]
	s_cmp_lg_u64 vcc, 0
	s_cselect_b32 s99, 1, 0
	v_mul_f32_e32 v2, 0xbe0293ee, v173
	v_fmamk_f32 v96, v96, 0x3e0293ee, v2
	s_waitcnt lgkmcnt(15)
	v_mfma_f32_32x32x16_bf16 v[64:79], v[184:187], v[208:211], v[64:79]
	ds_read_b128 v[208:211], v246
	v_fmamk_f32 v97, v97, 0x3e0293ee, v2
	v_fmamk_f32 v98, v98, 0x3e0293ee, v2
	v_fmamk_f32 v99, v99, 0x3e0293ee, v2
	v_fmamk_f32 v100, v100, 0x3e0293ee, v2
	v_fmamk_f32 v101, v101, 0x3e0293ee, v2
	v_fmamk_f32 v102, v102, 0x3e0293ee, v2
	s_waitcnt lgkmcnt(15)
	v_mfma_f32_32x32x16_bf16 v[48:63], v[184:187], v[212:215], v[48:63]
	ds_read_b128 v[212:215], v246 offset:8192
	v_fmamk_f32 v103, v103, 0x3e0293ee, v2
	v_fmamk_f32 v104, v104, 0x3e0293ee, v2
	v_fmamk_f32 v105, v105, 0x3e0293ee, v2
	v_fmamk_f32 v106, v106, 0x3e0293ee, v2
	v_fmamk_f32 v107, v107, 0x3e0293ee, v2
	v_fmamk_f32 v108, v108, 0x3e0293ee, v2
	s_waitcnt lgkmcnt(15)
	v_mfma_f32_32x32x16_bf16 v[32:47], v[184:187], v[216:219], v[32:47]
	ds_read_b128 v[216:219], v247
	v_fmamk_f32 v109, v109, 0x3e0293ee, v2
	v_fmamk_f32 v110, v110, 0x3e0293ee, v2
	v_fmamk_f32 v111, v111, 0x3e0293ee, v2
	v_exp_f32_e32 v96, v96
	v_fmamk_f32 v80, v80, 0x3e0293ee, v2
	s_waitcnt lgkmcnt(14)
	v_mfma_f32_32x32x16_bf16 v[16:31], v[184:187], v[220:223], v[16:31]
	ds_read_b128 v[220:223], v247 offset:8192
	ds_read_b128 v[184:187], v152 offset:64
	v_exp_f32_e32 v97, v97
	v_fmamk_f32 v81, v81, 0x3e0293ee, v2
	v_exp_f32_e32 v98, v98
	v_fmamk_f32 v82, v82, 0x3e0293ee, v2
	s_waitcnt lgkmcnt(12)
	v_mfma_f32_32x32x16_bf16 v[64:79], v[188:191], v[224:227], v[64:79]
	ds_read_b128 v[224:227], v248
	v_exp_f32_e32 v99, v99
	v_fmamk_f32 v83, v83, 0x3e0293ee, v2
	v_exp_f32_e32 v100, v100
	v_fmamk_f32 v84, v84, 0x3e0293ee, v2
	s_waitcnt lgkmcnt(11)
	v_mfma_f32_32x32x16_bf16 v[48:63], v[188:191], v[234:237], v[48:63]
	ds_read_b128 v[234:237], v248 offset:8192
	v_exp_f32_e32 v101, v101
	v_fmamk_f32 v85, v85, 0x3e0293ee, v2
	v_exp_f32_e32 v102, v102
	v_fmamk_f32 v86, v86, 0x3e0293ee, v2
	s_waitcnt lgkmcnt(10)
	v_mfma_f32_32x32x16_bf16 v[32:47], v[188:191], v[238:241], v[32:47]
	ds_read_b128 v[238:241], v249
	v_exp_f32_e32 v103, v103
	v_fmamk_f32 v87, v87, 0x3e0293ee, v2
	v_exp_f32_e32 v104, v104
	v_fmamk_f32 v88, v88, 0x3e0293ee, v2
	s_waitcnt lgkmcnt(9)
	v_mfma_f32_32x32x16_bf16 v[16:31], v[188:191], v[242:245], v[16:31]
	ds_read_b128 v[242:245], v249 offset:8192
	ds_read_b128 v[188:191], v152 offset:96
	v_exp_f32_e32 v105, v105
	v_fmamk_f32 v89, v89, 0x3e0293ee, v2
	v_exp_f32_e32 v106, v106
	v_fmamk_f32 v90, v90, 0x3e0293ee, v2
	v_exp_f32_e32 v107, v107
	v_fmamk_f32 v91, v91, 0x3e0293ee, v2
	v_exp_f32_e32 v108, v108
	v_fmamk_f32 v92, v92, 0x3e0293ee, v2
	v_exp_f32_e32 v109, v109
	v_fmamk_f32 v93, v93, 0x3e0293ee, v2
	v_exp_f32_e32 v110, v110
	v_fmamk_f32 v94, v94, 0x3e0293ee, v2
	v_exp_f32_e32 v111, v111
	v_fmamk_f32 v95, v95, 0x3e0293ee, v2
	s_branch .Lat_turn_end1

	.amdhsa_kernel _Z6mk_fwd6Params
		.amdhsa_group_segment_fixed_size 0
		.amdhsa_private_segment_fixed_size 0
		.amdhsa_kernarg_size 424
		.amdhsa_user_sgpr_count 2
		.amdhsa_user_sgpr_dispatch_ptr 0
		.amdhsa_user_sgpr_queue_ptr 0
		.amdhsa_user_sgpr_kernarg_segment_ptr 1
		.amdhsa_user_sgpr_dispatch_id 0
		.amdhsa_user_sgpr_kernarg_preload_length 0
		.amdhsa_user_sgpr_kernarg_preload_offset 0
		.amdhsa_user_sgpr_private_segment_size 0
		.amdhsa_uses_dynamic_stack 0
		.amdhsa_enable_private_segment 0
		.amdhsa_system_sgpr_workgroup_id_x 1
		.amdhsa_system_sgpr_workgroup_id_y 0
		.amdhsa_system_sgpr_workgroup_id_z 0
		.amdhsa_system_sgpr_workgroup_info 0
		.amdhsa_system_vgpr_workitem_id 0
		.amdhsa_next_free_vgpr 256
		.amdhsa_next_free_sgpr 102
		.amdhsa_accum_offset 256
		.amdhsa_reserve_vcc 1
		.amdhsa_float_round_mode_32 0
		.amdhsa_float_round_mode_16_64 0
		.amdhsa_float_denorm_mode_32 3
		.amdhsa_float_denorm_mode_16_64 3
		.amdhsa_dx10_clamp 1
		.amdhsa_ieee_mode 1
		.amdhsa_fp16_overflow 0
		.amdhsa_tg_split 0
		.amdhsa_exception_fp_ieee_invalid_op 0
		.amdhsa_exception_fp_denorm_src 0
		.amdhsa_exception_fp_ieee_div_zero 0
		.amdhsa_exception_fp_ieee_overflow 0
		.amdhsa_exception_fp_ieee_underflow 0
		.amdhsa_exception_fp_ieee_inexact 0
		.amdhsa_exception_int_div_zero 0
	.end_amdhsa_kernel

.Lfunc_end0:
	.size	_Z6mk_fwd6Params, .Lfunc_end0-_Z6mk_fwd6Params
	.set _Z6mk_fwd6Params.num_vgpr, 256
	.set _Z6mk_fwd6Params.num_agpr, 0
	.set _Z6mk_fwd6Params.numbered_sgpr, 102
	.set _Z6mk_fwd6Params.num_named_barrier, 0
	.set _Z6mk_fwd6Params.private_seg_size, 0
	.set _Z6mk_fwd6Params.uses_vcc, 1
	.set _Z6mk_fwd6Params.uses_flat_scratch, 0
	.set _Z6mk_fwd6Params.has_dyn_sized_stack, 0
	.set _Z6mk_fwd6Params.has_recursion, 0
	.set _Z6mk_fwd6Params.has_indirect_call, 0

amdhsa.kernels:
  - .agpr_count:     0
    .args:
      - .offset:         0
        .size:           168
        .value_kind:     by_value
      - .offset:         168
        .size:           4
        .value_kind:     hidden_block_count_x
      - .offset:         172
        .size:           4
        .value_kind:     hidden_block_count_y
      - .offset:         176
        .size:           4
        .value_kind:     hidden_block_count_z
      - .offset:         180
        .size:           2
        .value_kind:     hidden_group_size_x
      - .offset:         182
        .size:           2
        .value_kind:     hidden_group_size_y
      - .offset:         184
        .size:           2
        .value_kind:     hidden_group_size_z
      - .offset:         186
        .size:           2
        .value_kind:     hidden_remainder_x
      - .offset:         188
        .size:           2
        .value_kind:     hidden_remainder_y
      - .offset:         190
        .size:           2
        .value_kind:     hidden_remainder_z
      - .offset:         208
        .size:           8
        .value_kind:     hidden_global_offset_x
      - .offset:         216
        .size:           8
        .value_kind:     hidden_global_offset_y
      - .offset:         224
        .size:           8
        .value_kind:     hidden_global_offset_z
      - .offset:         232
        .size:           2
        .value_kind:     hidden_grid_dims
      - .offset:         288
        .size:           4
        .value_kind:     hidden_dynamic_lds_size
    .group_segment_fixed_size: 0
    .kernarg_segment_align: 8
    .kernarg_segment_size: 424
    .language:       OpenCL C
    .language_version:
      - 2
      - 0
    .max_flat_workgroup_size: 512
    .name:           _Z6mk_fwd6Params
    .private_segment_fixed_size: 0
    .sgpr_count:     108
    .sgpr_spill_count: 66
    .symbol:         _Z6mk_fwd6Params.kd
    .uniform_work_group_size: 1
    .uses_dynamic_stack: false
    .vgpr_count:     256
    .vgpr_spill_count: 0
    .wavefront_size: 64
